# prologue x->bf16 copy: eight loads in flight per wave with counted vmcnt instead of one load->vmcnt(0)->store round trip per iteration
# speedup vs baseline: 1.0014x; 1.0014x over previous
; __device__ __forceinline__ unsigned pk2(float lo, float hi) { return hw_pk_bf16(lo, hi); }
; __device__ __forceinline__ void p0_prologue(const Frame& F, const Args& a_) {
;     ...
;     { const f32x4* x4 = (const f32x4*)a.in[0]; u32x2* o = (u32x2*)(ws + WS_XB);
;       for (size_t i = gt; i < (size_t)T * D / 4; i += NGT) { const f32x4 v = x4[i]; u32x2 w; w.x = pk2(v.x, v.y); w.y = pk2(v.z, v.w); o[i] = w; } }
.LBB0_6:
	s_or_b64 exec, exec, s[4:5]
	s_lshr_b32 s0, s0, 6
	s_cmp_lt_i32 s54, 1
	v_writelane_b32 v255, s0, 7
	s_cselect_b64 s[0:1], -1, 0
	s_cmp_gt_i32 s55, 0
	s_cselect_b64 s[2:3], -1, 0
	s_and_b64 s[0:1], s[0:1], s[2:3]
	v_writelane_b32 v255, s48, 8
	s_andn2_b64 vcc, exec, s[0:1]
	v_readfirstlane_b32 s50, v0
	v_writelane_b32 v255, s49, 9
	s_cbranch_vccnz .LBB0_237
	v_readlane_b32 s0, v255, 4
	s_lshl_b32 s0, s0, 3
	v_readlane_b32 s1, v255, 7
	s_add_i32 s2, s0, s1
	s_load_dword s0, s[48:49], 0x128
	s_mov_b64 s[8:9], s[48:49]
	v_mov_b32_e32 v0, 0
	s_load_dwordx2 s[16:17], s[8:9], 0x118
	s_waitcnt lgkmcnt(0)
	s_lshl_b32 s22, s0, 9
	v_mbcnt_lo_u32_b32 v0, -1, v0
	v_mbcnt_hi_u32_b32 v0, -1, v0
	s_mov_b32 s0, 0x800000
	v_lshl_add_u32 v0, s2, 6, v0
	s_ashr_i32 s23, s22, 31
	v_mov_b32_e32 v1, 0
	v_cmp_gt_u32_e32 vcc, s0, v0
	s_and_saveexec_b64 s[4:5], vcc
	s_cbranch_execz .LBB0_10
	s_load_dwordx2 s[0:1], s[8:9], 0x0
	v_lshl_add_u64 v[2:3], v[0:1], 3, s[16:17]
	s_mov_b64 s[6:7], 0x35100000
	v_lshl_add_u64 v[2:3], v[2:3], 0, s[6:7]
	s_lshl_b64 s[6:7], s[22:23], 3
	s_waitcnt lgkmcnt(0)
	v_lshl_add_u64 v[4:5], v[0:1], 4, s[0:1]
	s_lshl_b64 s[10:11], s[22:23], 4
	v_mov_b64_e32 v[6:7], v[0:1]
	s_lshl_b32 s12, s22, 3
	s_mov_b32 s13, 0
	s_lshl_b32 s14, s2, 6
.Lxb_main:
	s_sub_u32 s15, s12, s22
	s_add_u32 s15, s15, s14
	s_cmp_lt_u32 s15, 0x800000
	s_cbranch_scc0 .Lxb_rest
	global_load_dwordx4 v[8:11], v[4:5], off
	v_lshl_add_u64 v[4:5], v[4:5], 0, s[10:11]
	global_load_dwordx4 v[12:15], v[4:5], off
	v_lshl_add_u64 v[4:5], v[4:5], 0, s[10:11]
	global_load_dwordx4 v[16:19], v[4:5], off
	v_lshl_add_u64 v[4:5], v[4:5], 0, s[10:11]
	global_load_dwordx4 v[20:23], v[4:5], off
	v_lshl_add_u64 v[4:5], v[4:5], 0, s[10:11]
	global_load_dwordx4 v[24:27], v[4:5], off
	v_lshl_add_u64 v[4:5], v[4:5], 0, s[10:11]
	global_load_dwordx4 v[28:31], v[4:5], off
	v_lshl_add_u64 v[4:5], v[4:5], 0, s[10:11]
	global_load_dwordx4 v[32:35], v[4:5], off
	v_lshl_add_u64 v[4:5], v[4:5], 0, s[10:11]
	global_load_dwordx4 v[36:39], v[4:5], off
	v_lshl_add_u64 v[4:5], v[4:5], 0, s[10:11]
	v_lshl_add_u64 v[6:7], v[6:7], 0, s[12:13]
	s_add_u32 s14, s14, s12
	s_waitcnt vmcnt(7)
	v_cvt_pk_bf16_f32 v8, v8, v9
	v_cvt_pk_bf16_f32 v9, v10, v11
	global_store_dwordx2 v[2:3], v[8:9], off
	v_lshl_add_u64 v[2:3], v[2:3], 0, s[6:7]
	s_waitcnt vmcnt(7)
	v_cvt_pk_bf16_f32 v12, v12, v13
	v_cvt_pk_bf16_f32 v13, v14, v15
	global_store_dwordx2 v[2:3], v[12:13], off
	v_lshl_add_u64 v[2:3], v[2:3], 0, s[6:7]
	s_waitcnt vmcnt(7)
	v_cvt_pk_bf16_f32 v16, v16, v17
	v_cvt_pk_bf16_f32 v17, v18, v19
	global_store_dwordx2 v[2:3], v[16:17], off
	v_lshl_add_u64 v[2:3], v[2:3], 0, s[6:7]
	s_waitcnt vmcnt(7)
	v_cvt_pk_bf16_f32 v20, v20, v21
	v_cvt_pk_bf16_f32 v21, v22, v23
	global_store_dwordx2 v[2:3], v[20:21], off
	v_lshl_add_u64 v[2:3], v[2:3], 0, s[6:7]
	s_waitcnt vmcnt(7)
	v_cvt_pk_bf16_f32 v24, v24, v25
	v_cvt_pk_bf16_f32 v25, v26, v27
	global_store_dwordx2 v[2:3], v[24:25], off
	v_lshl_add_u64 v[2:3], v[2:3], 0, s[6:7]
	s_waitcnt vmcnt(7)
	v_cvt_pk_bf16_f32 v28, v28, v29
	v_cvt_pk_bf16_f32 v29, v30, v31
	global_store_dwordx2 v[2:3], v[28:29], off
	v_lshl_add_u64 v[2:3], v[2:3], 0, s[6:7]
	s_waitcnt vmcnt(7)
	v_cvt_pk_bf16_f32 v32, v32, v33
	v_cvt_pk_bf16_f32 v33, v34, v35
	global_store_dwordx2 v[2:3], v[32:33], off
	v_lshl_add_u64 v[2:3], v[2:3], 0, s[6:7]
	s_waitcnt vmcnt(7)
	v_cvt_pk_bf16_f32 v36, v36, v37
	v_cvt_pk_bf16_f32 v37, v38, v39
	global_store_dwordx2 v[2:3], v[36:37], off
	v_lshl_add_u64 v[2:3], v[2:3], 0, s[6:7]
	s_branch .Lxb_main
.Lxb_rest:
	s_cmp_lt_u32 s14, 0x800000
	s_cbranch_scc0 .LBB0_10
	s_mov_b64 s[12:13], 0
	s_mov_b64 s[14:15], 0x7fffff
